# F1 + P.V segment of the second half-trip: 8 v_pk_fma_f32 with scalar-broadcast operands un-packed into 16 v_fmamk_f32 (same fma per element)
# speedup vs baseline: 1.0055x; 1.0055x over previous
.LBB0_761:
	s_waitcnt vmcnt(0) lgkmcnt(0)
	s_barrier
	ds_read_b128 v[64:67], v180 offset:32768
	ds_read_b128 v[68:71], v180 offset:40960
	ds_read_b128 v[222:225], v181 offset:32768
	ds_read_b128 v[226:229], v181 offset:40960
	ds_read_b128 v[230:233], v182 offset:32768
	ds_read_b128 v[234:237], v182 offset:40960
	ds_read_b128 v[238:241], v183 offset:32768
	ds_read_b128 v[242:245], v183 offset:40960
	v_exp_f32_e32 v164, v215
	v_add_f32_e32 v215, 0, v128
	s_waitcnt lgkmcnt(7)
	v_mfma_f32_32x32x16_bf16 v[80:95], v[64:67], v[124:127], 0
	s_add_i32 s80, s10, 64
	s_cmp_lt_u32 s12, 2
	s_cselect_b32 s80, s80, s11
	s_mul_i32 s81, s80, 0xc00
	s_add_i32 s85, s82, 0xc000
	s_mov_b32 m0, s85
	s_add_i32 s85, s82, 0x12000
	buffer_load_dwordx4 v154, s[72:75], s81 offen lds
	v_add_f32_e32 v215, v198, v215
	v_add_f32_e32 v215, v129, v215
	v_add_f32_e32 v215, v163, v215
	v_add_f32_e32 v215, v130, v215
	v_add_f32_e32 v215, v162, v215
	v_add_f32_e32 v215, v131, v215
	v_add_f32_e32 v215, v161, v215
	s_waitcnt lgkmcnt(6)
	v_mfma_f32_32x32x16_bf16 v[64:79], v[68:71], v[124:127], 0
	s_mov_b32 m0, s85
	s_add_i32 s85, s82, 0xe000
	buffer_load_dwordx4 v155, s[72:75], s81 offen lds
	v_add_f32_e32 v215, v132, v215
	v_add_f32_e32 v215, v139, v215
	v_add_f32_e32 v215, v133, v215
	v_add_f32_e32 v215, v138, v215
	v_add_f32_e32 v215, v134, v215
	v_exp_f32_e32 v165, v216
	v_add_f32_e32 v215, v137, v215
	s_waitcnt lgkmcnt(5)
	v_mfma_f32_32x32x16_bf16 v[80:95], v[222:225], v[120:123], v[80:95]
	s_mov_b32 m0, s85
	s_add_i32 s81, s81, 0x18000
	buffer_load_dwordx4 v154, s[72:75], s81 offen lds
	v_exp_f32_e32 v217, v217
	v_add_f32_e32 v215, v135, v215
	v_exp_f32_e32 v218, v218
	v_add_f32_e32 v215, v136, v215
	v_exp_f32_e32 v219, v219
	v_add_f32_e32 v215, v164, v215
	v_exp_f32_e32 v208, v208
	s_waitcnt lgkmcnt(4)
	v_mfma_f32_32x32x16_bf16 v[64:79], v[226:229], v[120:123], v[64:79]
	s_lshl_b32 s81, s84, 11
	s_add_i32 s85, s82, 0x0
	s_mov_b32 m0, s85
	s_add_i32 s85, s82, 0x2000
	buffer_load_dwordx4 v158, s[76:79], s81 offen lds
	ds_read_b128 v[222:225], v184 offset:32768
	ds_read_b128 v[226:229], v184 offset:40960
	v_add_f32_e32 v215, v165, v215
	v_exp_f32_e32 v209, v209
	v_add_f32_e32 v215, v217, v215
	v_exp_f32_e32 v210, v210
	v_add_f32_e32 v215, v218, v215
	v_exp_f32_e32 v211, v211
	s_waitcnt lgkmcnt(5)
	v_mfma_f32_32x32x16_bf16 v[80:95], v[230:233], v[116:119], v[80:95]
	s_mov_b32 m0, s85
	s_add_i32 s81, s81, 0x10000
	buffer_load_dwordx4 v158, s[76:79], s81 offen lds
	s_mov_b32 s83, s80
	v_add_f32_e32 v215, v219, v215
	v_exp_f32_e32 v212, v212
	v_add_f32_e32 v215, v208, v215
	v_exp_f32_e32 v213, v213
	v_add_f32_e32 v215, v209, v215
	v_exp_f32_e32 v214, v214
	v_add_f32_e32 v215, v210, v215
	s_waitcnt lgkmcnt(4)
	v_mfma_f32_32x32x16_bf16 v[64:79], v[234:237], v[116:119], v[64:79]
	ds_read_b128 v[230:233], v185 offset:32768
	ds_read_b128 v[234:237], v185 offset:40960
	v_exp_f32_e32 v207, v207
	v_add_f32_e32 v215, v211, v215
	v_exp_f32_e32 v220, v220
	v_add_f32_e32 v215, v212, v215
	v_exp_f32_e32 v221, v221
	v_add_f32_e32 v215, v213, v215
	s_waitcnt lgkmcnt(5)
	v_mfma_f32_32x32x16_bf16 v[80:95], v[238:241], v[112:115], v[80:95]
	v_exp_f32_e32 v205, v205
	v_add_f32_e32 v215, v214, v215
	v_add_f32_e32 v215, v207, v215
	v_add_f32_e32 v215, v220, v215
	v_add_f32_e32 v215, v221, v215
	v_add_f32_e32 v215, v205, v215
	v_mov_b32_e32 v216, v215
	s_waitcnt lgkmcnt(4)
	v_mfma_f32_32x32x16_bf16 v[64:79], v[242:245], v[112:115], v[64:79]
	ds_read_b128 v[238:241], v186 offset:32768
	ds_read_b128 v[242:245], v186 offset:40960
	v_permlane32_swap_b32_e32 v215, v216
	v_cvt_pk_bf16_f32 v128, v128, v198
	v_cvt_pk_bf16_f32 v129, v129, v163
	v_cvt_pk_bf16_f32 v130, v130, v162
	v_cvt_pk_bf16_f32 v131, v131, v161
	s_waitcnt lgkmcnt(5)
	v_mfma_f32_32x32x16_bf16 v[80:95], v[222:225], v[108:111], v[80:95]
	v_cvt_pk_bf16_f32 v132, v132, v139
	v_cvt_pk_bf16_f32 v133, v133, v138
	v_cvt_pk_bf16_f32 v134, v134, v137
	v_cvt_pk_bf16_f32 v135, v135, v136
	v_cvt_pk_bf16_f32 v136, v164, v165
	v_cvt_pk_bf16_f32 v137, v217, v218
	v_cvt_pk_bf16_f32 v138, v219, v208
	s_waitcnt lgkmcnt(4)
	v_mfma_f32_32x32x16_bf16 v[64:79], v[226:229], v[108:111], v[64:79]
	ds_read_b128 v[222:225], v187 offset:32768
	ds_read_b128 v[226:229], v187 offset:40960
	v_cvt_pk_bf16_f32 v139, v209, v210
	v_cvt_pk_bf16_f32 v208, v211, v212
	v_cvt_pk_bf16_f32 v209, v213, v214
	v_cvt_pk_bf16_f32 v210, v207, v220
	v_cvt_pk_bf16_f32 v211, v221, v205
	v_permlane32_swap_b32_e32 v128, v130
	s_waitcnt lgkmcnt(5)
	v_mfma_f32_32x32x16_bf16 v[80:95], v[230:233], v[104:107], v[80:95]
	v_permlane32_swap_b32_e32 v129, v131
	v_permlane32_swap_b32_e32 v132, v134
	v_permlane32_swap_b32_e32 v133, v135
	v_permlane32_swap_b32_e32 v136, v138
	s_waitcnt lgkmcnt(4)
	v_mfma_f32_32x32x16_bf16 v[64:79], v[234:237], v[104:107], v[64:79]
	ds_read_b128 v[230:233], v191
	ds_read_b128 v[234:237], v191 offset:4096
	ds_read_b128 v[246:249], v190
	v_permlane32_swap_b32_e32 v137, v139
	v_permlane32_swap_b32_e32 v208, v210
	v_permlane32_swap_b32_e32 v209, v211
	s_waitcnt lgkmcnt(6)
	v_mfma_f32_32x32x16_bf16 v[80:95], v[238:241], v[100:103], v[80:95]
	s_waitcnt lgkmcnt(5)
	v_mfma_f32_32x32x16_bf16 v[64:79], v[242:245], v[100:103], v[64:79]
	ds_read_b128 v[238:241], v192
	ds_read_b128 v[242:245], v192 offset:4096
	ds_read_b128 v[250:253], v190 offset:1024
	s_waitcnt lgkmcnt(7)
	v_mfma_f32_32x32x16_bf16 v[80:95], v[222:225], v[96:99], v[80:95]
	s_waitcnt lgkmcnt(6)
	v_mfma_f32_32x32x16_bf16 v[64:79], v[226:229], v[96:99], v[64:79]
	ds_read_b128 v[222:225], v193
	ds_read_b128 v[226:229], v193 offset:4096
	s_waitcnt lgkmcnt(5)
	v_mfma_f32_32x32x16_bf16 v[80:95], v[230:233], v[246:249], v[80:95]
	s_waitcnt lgkmcnt(5)
	v_mfma_f32_32x32x16_bf16 v[64:79], v[234:237], v[246:249], v[64:79]
	ds_read_b128 v[230:233], v194
	ds_read_b128 v[234:237], v194 offset:4096
	ds_read_b128 v[246:249], v190 offset:2048
	s_waitcnt lgkmcnt(5)
	v_mfma_f32_32x32x16_bf16 v[80:95], v[238:241], v[250:253], v[80:95]
	s_waitcnt lgkmcnt(5)
	v_mfma_f32_32x32x16_bf16 v[64:79], v[242:245], v[250:253], v[64:79]
	ds_read_b128 v[250:253], v190 offset:3072
	s_waitcnt lgkmcnt(1)
	v_mfma_f32_32x32x16_bf16 v[80:95], v[222:225], v[246:249], v[80:95]
	s_waitcnt lgkmcnt(1)
	v_mfma_f32_32x32x16_bf16 v[64:79], v[226:229], v[246:249], v[64:79]
	s_waitcnt lgkmcnt(0)
	v_mfma_f32_32x32x16_bf16 v[80:95], v[230:233], v[250:253], v[80:95]
	s_waitcnt lgkmcnt(0)
	v_mfma_f32_32x32x16_bf16 v[64:79], v[234:237], v[250:253], v[64:79]
	ds_read_b64_tr_b16 v[238:239], v174 offset:0
	ds_read_b64_tr_b16 v[240:241], v174 offset:0x800
	ds_read_b64_tr_b16 v[242:243], v174 offset:0x1000
	ds_read_b64_tr_b16 v[244:245], v174 offset:0x1800
	ds_read_b64_tr_b16 v[246:247], v174 offset:0x2000
	ds_read_b64_tr_b16 v[248:249], v174 offset:0x2800
	ds_read_b64_tr_b16 v[250:251], v174 offset:0x3000
	ds_read_b64_tr_b16 v[252:253], v174 offset:0x3800
	s_nop 3
	v_max_f32_e32 v161, v81, v81
	v_max_f32_e32 v162, v80, v80
	v_max_f32_e32 v161, v162, v161
	v_max3_f32 v161, v161, v82, v83
	v_max3_f32 v161, v161, v84, v85
	v_max3_f32 v161, v161, v86, v87
	v_max3_f32 v161, v161, v88, v89
	v_max3_f32 v161, v161, v90, v91
	v_max3_f32 v161, v161, v92, v93
	v_max3_f32 v161, v161, v94, v95
	s_waitcnt lgkmcnt(0)
	v_mfma_f32_32x32x16_bf16 v[16:31], v[128:131], v[238:241], v[16:31]
	ds_read_b64_tr_b16 v[238:239], v174 offset:0x200
	ds_read_b64_tr_b16 v[240:241], v174 offset:0xa00
	v_max3_f32 v161, v161, v64, v65
	v_max3_f32 v161, v161, v66, v67
	v_max3_f32 v161, v161, v68, v69
	v_mfma_f32_32x32x16_bf16 v[16:31], v[132:135], v[242:245], v[16:31]
	ds_read_b64_tr_b16 v[242:243], v174 offset:0x1200
	ds_read_b64_tr_b16 v[244:245], v174 offset:0x1a00
	v_max3_f32 v161, v161, v70, v71
	v_max3_f32 v161, v161, v72, v73
	v_max3_f32 v161, v161, v74, v75
	v_mfma_f32_32x32x16_bf16 v[16:31], v[136:139], v[246:249], v[16:31]
	ds_read_b64_tr_b16 v[246:247], v174 offset:0x2200
	ds_read_b64_tr_b16 v[248:249], v174 offset:0x2a00
	ds_read_b64_tr_b16 v[162:163], v174 offset:0x3200
	ds_read_b64_tr_b16 v[164:165], v174 offset:0x3a00
	v_max3_f32 v161, v161, v76, v77
	v_max3_f32 v161, v161, v78, v79
	v_mov_b32_e32 v198, v161
	v_mfma_f32_32x32x16_bf16 v[16:31], v[208:211], v[250:253], v[16:31]
	v_max_f32_e32 v205, v160, v160
	v_permlane32_swap_b32_e32 v161, v198
	v_max_f32_e32 v198, v198, v198
	v_max_f32_e32 v161, v161, v161
	v_max_f32_e32 v161, v161, v198
	s_waitcnt lgkmcnt(0)
	v_mfma_f32_32x32x16_bf16 v[32:47], v[128:131], v[238:241], v[32:47]
	ds_read_b64_tr_b16 v[238:239], v174 offset:0x400
	ds_read_b64_tr_b16 v[240:241], v174 offset:0xc00
	v_sub_f32_e32 v198, v161, v160
	v_max_f32_e32 v161, v205, v161
	v_sub_f32_e32 v205, v160, v161
	v_mul_f32_e32 v205, 0x3dd53b94, v205
	v_exp_f32_e32 v205, v205
	v_mfma_f32_32x32x16_bf16 v[32:47], v[132:135], v[242:245], v[32:47]
	ds_read_b64_tr_b16 v[242:243], v174 offset:0x1400
	ds_read_b64_tr_b16 v[244:245], v174 offset:0x1c00
	v_cmp_ge_f32_e32 vcc, s48, v198
	s_cmp_eq_u64 vcc, exec
	s_cselect_b64 s[6:7], -1, 0
	v_cndmask_b32_e64 v205, v205, 1.0, s[6:7]
	v_cndmask_b32_e64 v198, v161, v160, s[6:7]
	v_mul_f32_e32 v236, 0xbdd53b94, v198
	v_mov_b32_e32 v237, v236
	v_cmp_gt_f32_e32 vcc, 1.0, v205
	v_mfma_f32_32x32x16_bf16 v[32:47], v[136:139], v[246:249], v[32:47]
	ds_read_b64_tr_b16 v[246:247], v174 offset:0x2400
	ds_read_b64_tr_b16 v[248:249], v174 offset:0x2c00
	ds_read_b64_tr_b16 v[250:251], v174 offset:0x3400
	ds_read_b64_tr_b16 v[252:253], v174 offset:0x3c00
	v_fmamk_f32 v80, v80, 0x3dd53b94, v236
	v_fmamk_f32 v81, v81, 0x3dd53b94, v236
	v_fmamk_f32 v82, v82, 0x3dd53b94, v236
	v_fmamk_f32 v83, v83, 0x3dd53b94, v236
	v_mfma_f32_32x32x16_bf16 v[32:47], v[208:211], v[162:165], v[32:47]
	v_fmamk_f32 v84, v84, 0x3dd53b94, v236
	v_fmamk_f32 v85, v85, 0x3dd53b94, v236
	v_fmamk_f32 v86, v86, 0x3dd53b94, v236
	v_fmamk_f32 v87, v87, 0x3dd53b94, v236
	s_waitcnt lgkmcnt(0)
	v_mfma_f32_32x32x16_bf16 v[0:15], v[128:131], v[238:241], v[0:15]
	ds_read_b64_tr_b16 v[162:163], v174 offset:0x600
	ds_read_b64_tr_b16 v[164:165], v174 offset:0xe00
	ds_read_b64_tr_b16 v[238:239], v174 offset:0x1600
	ds_read_b64_tr_b16 v[240:241], v174 offset:0x1e00
	v_fmamk_f32 v88, v88, 0x3dd53b94, v236
	v_fmamk_f32 v89, v89, 0x3dd53b94, v236
	v_fmamk_f32 v90, v90, 0x3dd53b94, v236
	v_fmamk_f32 v91, v91, 0x3dd53b94, v236
	v_mfma_f32_32x32x16_bf16 v[0:15], v[132:135], v[242:245], v[0:15]
	ds_read_b64_tr_b16 v[242:243], v174 offset:0x2600
	ds_read_b64_tr_b16 v[244:245], v174 offset:0x2e00
	v_fmamk_f32 v92, v92, 0x3dd53b94, v236
	v_fmamk_f32 v93, v93, 0x3dd53b94, v236
	v_fmamk_f32 v94, v94, 0x3dd53b94, v236
	v_fmamk_f32 v95, v95, 0x3dd53b94, v236
	v_mfma_f32_32x32x16_bf16 v[0:15], v[136:139], v[246:249], v[0:15]
	ds_read_b64_tr_b16 v[246:247], v174 offset:0x3600
	ds_read_b64_tr_b16 v[248:249], v174 offset:0x3e00
	v_exp_f32_e32 v222, v80
	v_exp_f32_e32 v224, v81
	v_exp_f32_e32 v220, v82
	v_mfma_f32_32x32x16_bf16 v[0:15], v[208:211], v[250:253], v[0:15]
	v_exp_f32_e32 v223, v83
	v_exp_f32_e32 v219, v84
	v_exp_f32_e32 v221, v85
	s_waitcnt lgkmcnt(0)
	v_mfma_f32_32x32x16_bf16 v[48:63], v[128:131], v[162:165], v[48:63]
	v_exp_f32_e32 v217, v86
	v_exp_f32_e32 v218, v87
	v_exp_f32_e32 v212, v88
	v_fmamk_f32 v130, v70, 0x3dd53b94, v236
	v_fmamk_f32 v131, v71, 0x3dd53b94, v236
	v_fmamk_f32 v128, v72, 0x3dd53b94, v236
	v_fmamk_f32 v129, v73, 0x3dd53b94, v236
	v_mfma_f32_32x32x16_bf16 v[48:63], v[132:135], v[238:241], v[48:63]
	v_exp_f32_e32 v214, v89
	v_exp_f32_e32 v213, v91
	v_exp_f32_e32 v207, v94
	v_fmamk_f32 v132, v68, 0x3dd53b94, v236
	v_fmamk_f32 v133, v69, 0x3dd53b94, v236
	v_fmamk_f32 v134, v78, 0x3dd53b94, v236
	v_fmamk_f32 v135, v79, 0x3dd53b94, v236
	v_mfma_f32_32x32x16_bf16 v[48:63], v[136:139], v[242:245], v[48:63]
	v_fmamk_f32 v138, v64, 0x3dd53b94, v236
	v_fmamk_f32 v139, v65, 0x3dd53b94, v236
	v_fmamk_f32 v136, v66, 0x3dd53b94, v236
	v_fmamk_f32 v137, v67, 0x3dd53b94, v236
	v_fmamk_f32 v162, v74, 0x3dd53b94, v236
	v_fmamk_f32 v163, v75, 0x3dd53b94, v236
	v_fmamk_f32 v160, v76, 0x3dd53b94, v236
	v_fmamk_f32 v161, v77, 0x3dd53b94, v236
	v_mfma_f32_32x32x16_bf16 v[48:63], v[208:211], v[246:249], v[48:63]
	v_exp_f32_e32 v211, v90
	v_exp_f32_e32 v208, v92
	v_exp_f32_e32 v210, v93
	v_exp_f32_e32 v209, v95
	v_add_f32_e32 v64, v203, v204
	v_fmac_f32_e32 v64, v197, v140
	v_add_f32_e32 v140, v215, v216
	s_addk_i32 s10, 0x80
	s_add_i32 s64, s64, 2
	s_addk_i32 s11, 0x80
	v_fmac_f32_e32 v140, v64, v206
	s_cbranch_vccz .LBB0_765
	s_and_saveexec_b64 s[8:9], s[4:5]
	ds_write_b32 v189, v205 offset:128
	s_or_b64 exec, exec, s[8:9]
	s_waitcnt lgkmcnt(0)
	v_add_u32_e32 v164, s62, v169
	ds_read_b128 v[238:241], v164 offset:224
	ds_read_b128 v[242:245], v164 offset:192
	ds_read_b128 v[246:249], v164 offset:160
	ds_read_b128 v[250:253], v164 offset:128
	s_waitcnt lgkmcnt(3)
	v_pk_mul_f32 v[28:29], v[28:29], v[238:239]
	s_waitcnt lgkmcnt(2)
	v_pk_mul_f32 v[24:25], v[24:25], v[242:243]
	s_waitcnt lgkmcnt(1)
	v_pk_mul_f32 v[20:21], v[20:21], v[246:247]
	v_pk_mul_f32 v[30:31], v[30:31], v[240:241]
	v_pk_mul_f32 v[26:27], v[26:27], v[244:245]
	v_pk_mul_f32 v[22:23], v[22:23], v[248:249]
	s_waitcnt lgkmcnt(0)
	v_pk_mul_f32 v[18:19], v[18:19], v[252:253]
	v_pk_mul_f32 v[16:17], v[16:17], v[250:251]
	v_pk_mul_f32 v[44:45], v[44:45], v[238:239]
	v_pk_mul_f32 v[40:41], v[40:41], v[242:243]
	v_pk_mul_f32 v[36:37], v[36:37], v[246:247]
	v_pk_mul_f32 v[46:47], v[46:47], v[240:241]
	v_pk_mul_f32 v[42:43], v[42:43], v[244:245]
	v_pk_mul_f32 v[38:39], v[38:39], v[248:249]
	v_pk_mul_f32 v[34:35], v[34:35], v[252:253]
	v_pk_mul_f32 v[32:33], v[32:33], v[250:251]
	v_pk_mul_f32 v[12:13], v[12:13], v[238:239]
	v_pk_mul_f32 v[8:9], v[8:9], v[242:243]
	v_pk_mul_f32 v[4:5], v[4:5], v[246:247]
	v_pk_mul_f32 v[14:15], v[14:15], v[240:241]
	v_pk_mul_f32 v[10:11], v[10:11], v[244:245]
	v_pk_mul_f32 v[6:7], v[6:7], v[248:249]
	v_pk_mul_f32 v[2:3], v[2:3], v[252:253]
	v_pk_mul_f32 v[0:1], v[0:1], v[250:251]
	v_pk_mul_f32 v[60:61], v[60:61], v[238:239]
	v_pk_mul_f32 v[56:57], v[56:57], v[242:243]
	v_pk_mul_f32 v[52:53], v[52:53], v[246:247]
	v_pk_mul_f32 v[62:63], v[62:63], v[240:241]
	v_pk_mul_f32 v[58:59], v[58:59], v[244:245]
	v_pk_mul_f32 v[54:55], v[54:55], v[248:249]
	v_pk_mul_f32 v[50:51], v[50:51], v[252:253]
	v_pk_mul_f32 v[48:49], v[48:49], v[250:251]

.LBB0_2016:
	s_waitcnt vmcnt(0) lgkmcnt(0)
	s_barrier
	ds_read_b128 v[64:67], v180 offset:32768
	ds_read_b128 v[68:71], v180 offset:40960
	ds_read_b128 v[222:225], v181 offset:32768
	ds_read_b128 v[226:229], v181 offset:40960
	ds_read_b128 v[230:233], v182 offset:32768
	ds_read_b128 v[234:237], v182 offset:40960
	ds_read_b128 v[238:241], v183 offset:32768
	ds_read_b128 v[242:245], v183 offset:40960
	v_exp_f32_e32 v164, v215
	v_add_f32_e32 v215, 0, v128
	s_waitcnt lgkmcnt(7)
	v_mfma_f32_32x32x16_bf16 v[80:95], v[64:67], v[124:127], 0
	s_add_i32 s80, s13, 64
	s_cmp_lt_u32 s8, 2
	s_cselect_b32 s80, s80, s14
	s_mul_i32 s81, s80, 0xc00
	s_add_i32 s85, s82, 0xc000
	s_mov_b32 m0, s85
	s_add_i32 s85, s82, 0x12000
	buffer_load_dwordx4 v154, s[72:75], s81 offen lds
	v_add_f32_e32 v215, v198, v215
	v_add_f32_e32 v215, v129, v215
	v_add_f32_e32 v215, v163, v215
	v_add_f32_e32 v215, v130, v215
	v_add_f32_e32 v215, v162, v215
	v_add_f32_e32 v215, v131, v215
	v_add_f32_e32 v215, v161, v215
	s_waitcnt lgkmcnt(6)
	v_mfma_f32_32x32x16_bf16 v[64:79], v[68:71], v[124:127], 0
	s_mov_b32 m0, s85
	s_add_i32 s85, s82, 0xe000
	buffer_load_dwordx4 v155, s[72:75], s81 offen lds
	v_add_f32_e32 v215, v132, v215
	v_add_f32_e32 v215, v139, v215
	v_add_f32_e32 v215, v133, v215
	v_add_f32_e32 v215, v138, v215
	v_add_f32_e32 v215, v134, v215
	v_exp_f32_e32 v165, v216
	v_add_f32_e32 v215, v137, v215
	s_waitcnt lgkmcnt(5)
	v_mfma_f32_32x32x16_bf16 v[80:95], v[222:225], v[120:123], v[80:95]
	s_mov_b32 m0, s85
	s_add_i32 s81, s81, 0x18000
	buffer_load_dwordx4 v154, s[72:75], s81 offen lds
	v_exp_f32_e32 v217, v217
	v_add_f32_e32 v215, v135, v215
	v_exp_f32_e32 v218, v218
	v_add_f32_e32 v215, v136, v215
	v_exp_f32_e32 v219, v219
	v_add_f32_e32 v215, v164, v215
	v_exp_f32_e32 v208, v208
	s_waitcnt lgkmcnt(4)
	v_mfma_f32_32x32x16_bf16 v[64:79], v[226:229], v[120:123], v[64:79]
	s_lshl_b32 s81, s84, 11
	s_add_i32 s85, s82, 0x0
	s_mov_b32 m0, s85
	s_add_i32 s85, s82, 0x2000
	buffer_load_dwordx4 v158, s[76:79], s81 offen lds
	ds_read_b128 v[222:225], v184 offset:32768
	ds_read_b128 v[226:229], v184 offset:40960
	v_add_f32_e32 v215, v165, v215
	v_exp_f32_e32 v209, v209
	v_add_f32_e32 v215, v217, v215
	v_exp_f32_e32 v210, v210
	v_add_f32_e32 v215, v218, v215
	v_exp_f32_e32 v211, v211
	s_waitcnt lgkmcnt(5)
	v_mfma_f32_32x32x16_bf16 v[80:95], v[230:233], v[116:119], v[80:95]
	s_mov_b32 m0, s85
	s_add_i32 s81, s81, 0x10000
	buffer_load_dwordx4 v158, s[76:79], s81 offen lds
	s_mov_b32 s83, s80
	v_add_f32_e32 v215, v219, v215
	v_exp_f32_e32 v212, v212
	v_add_f32_e32 v215, v208, v215
	v_exp_f32_e32 v213, v213
	v_add_f32_e32 v215, v209, v215
	v_exp_f32_e32 v214, v214
	v_add_f32_e32 v215, v210, v215
	s_waitcnt lgkmcnt(4)
	v_mfma_f32_32x32x16_bf16 v[64:79], v[234:237], v[116:119], v[64:79]
	ds_read_b128 v[230:233], v185 offset:32768
	ds_read_b128 v[234:237], v185 offset:40960
	v_exp_f32_e32 v207, v207
	v_add_f32_e32 v215, v211, v215
	v_exp_f32_e32 v220, v220
	v_add_f32_e32 v215, v212, v215
	v_exp_f32_e32 v221, v221
	v_add_f32_e32 v215, v213, v215
	s_waitcnt lgkmcnt(5)
	v_mfma_f32_32x32x16_bf16 v[80:95], v[238:241], v[112:115], v[80:95]
	v_exp_f32_e32 v205, v205
	v_add_f32_e32 v215, v214, v215
	v_add_f32_e32 v215, v207, v215
	v_add_f32_e32 v215, v220, v215
	v_add_f32_e32 v215, v221, v215
	v_add_f32_e32 v215, v205, v215
	v_mov_b32_e32 v216, v215
	s_waitcnt lgkmcnt(4)
	v_mfma_f32_32x32x16_bf16 v[64:79], v[242:245], v[112:115], v[64:79]
	ds_read_b128 v[238:241], v186 offset:32768
	ds_read_b128 v[242:245], v186 offset:40960
	v_permlane32_swap_b32_e32 v215, v216
	v_cvt_pk_bf16_f32 v128, v128, v198
	v_cvt_pk_bf16_f32 v129, v129, v163
	v_cvt_pk_bf16_f32 v130, v130, v162
	v_cvt_pk_bf16_f32 v131, v131, v161
	s_waitcnt lgkmcnt(5)
	v_mfma_f32_32x32x16_bf16 v[80:95], v[222:225], v[108:111], v[80:95]
	v_cvt_pk_bf16_f32 v132, v132, v139
	v_cvt_pk_bf16_f32 v133, v133, v138
	v_cvt_pk_bf16_f32 v134, v134, v137
	v_cvt_pk_bf16_f32 v135, v135, v136
	v_cvt_pk_bf16_f32 v136, v164, v165
	v_cvt_pk_bf16_f32 v137, v217, v218
	v_cvt_pk_bf16_f32 v138, v219, v208
	s_waitcnt lgkmcnt(4)
	v_mfma_f32_32x32x16_bf16 v[64:79], v[226:229], v[108:111], v[64:79]
	ds_read_b128 v[222:225], v187 offset:32768
	ds_read_b128 v[226:229], v187 offset:40960
	v_cvt_pk_bf16_f32 v139, v209, v210
	v_cvt_pk_bf16_f32 v208, v211, v212
	v_cvt_pk_bf16_f32 v209, v213, v214
	v_cvt_pk_bf16_f32 v210, v207, v220
	v_cvt_pk_bf16_f32 v211, v221, v205
	v_permlane32_swap_b32_e32 v128, v130
	s_waitcnt lgkmcnt(5)
	v_mfma_f32_32x32x16_bf16 v[80:95], v[230:233], v[104:107], v[80:95]
	v_permlane32_swap_b32_e32 v129, v131
	v_permlane32_swap_b32_e32 v132, v134
	v_permlane32_swap_b32_e32 v133, v135
	v_permlane32_swap_b32_e32 v136, v138
	s_waitcnt lgkmcnt(4)
	v_mfma_f32_32x32x16_bf16 v[64:79], v[234:237], v[104:107], v[64:79]
	ds_read_b128 v[230:233], v191
	ds_read_b128 v[234:237], v191 offset:4096
	ds_read_b128 v[246:249], v190
	v_permlane32_swap_b32_e32 v137, v139
	v_permlane32_swap_b32_e32 v208, v210
	v_permlane32_swap_b32_e32 v209, v211
	s_waitcnt lgkmcnt(6)
	v_mfma_f32_32x32x16_bf16 v[80:95], v[238:241], v[100:103], v[80:95]
	s_waitcnt lgkmcnt(5)
	v_mfma_f32_32x32x16_bf16 v[64:79], v[242:245], v[100:103], v[64:79]
	ds_read_b128 v[238:241], v192
	ds_read_b128 v[242:245], v192 offset:4096
	ds_read_b128 v[250:253], v190 offset:1024
	s_waitcnt lgkmcnt(7)
	v_mfma_f32_32x32x16_bf16 v[80:95], v[222:225], v[96:99], v[80:95]
	s_waitcnt lgkmcnt(6)
	v_mfma_f32_32x32x16_bf16 v[64:79], v[226:229], v[96:99], v[64:79]
	ds_read_b128 v[222:225], v193
	ds_read_b128 v[226:229], v193 offset:4096
	s_waitcnt lgkmcnt(5)
	v_mfma_f32_32x32x16_bf16 v[80:95], v[230:233], v[246:249], v[80:95]
	s_waitcnt lgkmcnt(5)
	v_mfma_f32_32x32x16_bf16 v[64:79], v[234:237], v[246:249], v[64:79]
	ds_read_b128 v[230:233], v194
	ds_read_b128 v[234:237], v194 offset:4096
	ds_read_b128 v[246:249], v190 offset:2048
	s_waitcnt lgkmcnt(5)
	v_mfma_f32_32x32x16_bf16 v[80:95], v[238:241], v[250:253], v[80:95]
	s_waitcnt lgkmcnt(5)
	v_mfma_f32_32x32x16_bf16 v[64:79], v[242:245], v[250:253], v[64:79]
	ds_read_b128 v[250:253], v190 offset:3072
	s_waitcnt lgkmcnt(1)
	v_mfma_f32_32x32x16_bf16 v[80:95], v[222:225], v[246:249], v[80:95]
	s_waitcnt lgkmcnt(1)
	v_mfma_f32_32x32x16_bf16 v[64:79], v[226:229], v[246:249], v[64:79]
	s_waitcnt lgkmcnt(0)
	v_mfma_f32_32x32x16_bf16 v[80:95], v[230:233], v[250:253], v[80:95]
	s_waitcnt lgkmcnt(0)
	v_mfma_f32_32x32x16_bf16 v[64:79], v[234:237], v[250:253], v[64:79]
	ds_read_b64_tr_b16 v[238:239], v174 offset:0
	ds_read_b64_tr_b16 v[240:241], v174 offset:0x800
	ds_read_b64_tr_b16 v[242:243], v174 offset:0x1000
	ds_read_b64_tr_b16 v[244:245], v174 offset:0x1800
	ds_read_b64_tr_b16 v[246:247], v174 offset:0x2000
	ds_read_b64_tr_b16 v[248:249], v174 offset:0x2800
	ds_read_b64_tr_b16 v[250:251], v174 offset:0x3000
	ds_read_b64_tr_b16 v[252:253], v174 offset:0x3800
	s_nop 3
	v_max_f32_e32 v161, v81, v81
	v_max_f32_e32 v162, v80, v80
	v_max_f32_e32 v161, v162, v161
	v_max3_f32 v161, v161, v82, v83
	v_max3_f32 v161, v161, v84, v85
	v_max3_f32 v161, v161, v86, v87
	v_max3_f32 v161, v161, v88, v89
	v_max3_f32 v161, v161, v90, v91
	v_max3_f32 v161, v161, v92, v93
	v_max3_f32 v161, v161, v94, v95
	s_waitcnt lgkmcnt(0)
	v_mfma_f32_32x32x16_bf16 v[0:15], v[128:131], v[238:241], v[0:15]
	ds_read_b64_tr_b16 v[238:239], v174 offset:0x200
	ds_read_b64_tr_b16 v[240:241], v174 offset:0xa00
	v_max3_f32 v161, v161, v64, v65
	v_max3_f32 v161, v161, v66, v67
	v_max3_f32 v161, v161, v68, v69
	v_mfma_f32_32x32x16_bf16 v[0:15], v[132:135], v[242:245], v[0:15]
	ds_read_b64_tr_b16 v[242:243], v174 offset:0x1200
	ds_read_b64_tr_b16 v[244:245], v174 offset:0x1a00
	v_max3_f32 v161, v161, v70, v71
	v_max3_f32 v161, v161, v72, v73
	v_max3_f32 v161, v161, v74, v75
	v_mfma_f32_32x32x16_bf16 v[0:15], v[136:139], v[246:249], v[0:15]
	ds_read_b64_tr_b16 v[246:247], v174 offset:0x2200
	ds_read_b64_tr_b16 v[248:249], v174 offset:0x2a00
	ds_read_b64_tr_b16 v[162:163], v174 offset:0x3200
	ds_read_b64_tr_b16 v[164:165], v174 offset:0x3a00
	v_max3_f32 v161, v161, v76, v77
	v_max3_f32 v161, v161, v78, v79
	v_mov_b32_e32 v198, v161
	v_mfma_f32_32x32x16_bf16 v[0:15], v[208:211], v[250:253], v[0:15]
	v_max_f32_e32 v205, v160, v160
	v_permlane32_swap_b32_e32 v161, v198
	v_max_f32_e32 v198, v198, v198
	v_max_f32_e32 v161, v161, v161
	v_max_f32_e32 v161, v161, v198
	s_waitcnt lgkmcnt(0)
	v_mfma_f32_32x32x16_bf16 v[32:47], v[128:131], v[238:241], v[32:47]
	ds_read_b64_tr_b16 v[238:239], v174 offset:0x400
	ds_read_b64_tr_b16 v[240:241], v174 offset:0xc00
	v_sub_f32_e32 v198, v161, v160
	v_max_f32_e32 v161, v205, v161
	v_sub_f32_e32 v205, v160, v161
	v_mul_f32_e32 v205, 0x3dd53b94, v205
	v_exp_f32_e32 v205, v205
	v_mfma_f32_32x32x16_bf16 v[32:47], v[132:135], v[242:245], v[32:47]
	ds_read_b64_tr_b16 v[242:243], v174 offset:0x1400
	ds_read_b64_tr_b16 v[244:245], v174 offset:0x1c00
	v_cmp_ge_f32_e32 vcc, s46, v198
	s_cmp_eq_u64 vcc, exec
	s_cselect_b64 s[6:7], -1, 0
	v_cndmask_b32_e64 v205, v205, 1.0, s[6:7]
	v_cndmask_b32_e64 v198, v161, v160, s[6:7]
	v_mul_f32_e32 v236, 0xbdd53b94, v198
	v_mov_b32_e32 v237, v236
	v_cmp_gt_f32_e32 vcc, 1.0, v205
	v_mfma_f32_32x32x16_bf16 v[32:47], v[136:139], v[246:249], v[32:47]
	ds_read_b64_tr_b16 v[246:247], v174 offset:0x2400
	ds_read_b64_tr_b16 v[248:249], v174 offset:0x2c00
	ds_read_b64_tr_b16 v[250:251], v174 offset:0x3400
	ds_read_b64_tr_b16 v[252:253], v174 offset:0x3c00
	v_fmamk_f32 v80, v80, 0x3dd53b94, v236
	v_fmamk_f32 v81, v81, 0x3dd53b94, v236
	v_fmamk_f32 v82, v82, 0x3dd53b94, v236
	v_fmamk_f32 v83, v83, 0x3dd53b94, v236
	v_mfma_f32_32x32x16_bf16 v[32:47], v[208:211], v[162:165], v[32:47]
	v_fmamk_f32 v84, v84, 0x3dd53b94, v236
	v_fmamk_f32 v85, v85, 0x3dd53b94, v236
	v_fmamk_f32 v86, v86, 0x3dd53b94, v236
	v_fmamk_f32 v87, v87, 0x3dd53b94, v236
	s_waitcnt lgkmcnt(0)
	v_mfma_f32_32x32x16_bf16 v[16:31], v[128:131], v[238:241], v[16:31]
	ds_read_b64_tr_b16 v[162:163], v174 offset:0x600
	ds_read_b64_tr_b16 v[164:165], v174 offset:0xe00
	ds_read_b64_tr_b16 v[238:239], v174 offset:0x1600
	ds_read_b64_tr_b16 v[240:241], v174 offset:0x1e00
	v_fmamk_f32 v88, v88, 0x3dd53b94, v236
	v_fmamk_f32 v89, v89, 0x3dd53b94, v236
	v_fmamk_f32 v90, v90, 0x3dd53b94, v236
	v_fmamk_f32 v91, v91, 0x3dd53b94, v236
	v_mfma_f32_32x32x16_bf16 v[16:31], v[132:135], v[242:245], v[16:31]
	ds_read_b64_tr_b16 v[242:243], v174 offset:0x2600
	ds_read_b64_tr_b16 v[244:245], v174 offset:0x2e00
	v_fmamk_f32 v92, v92, 0x3dd53b94, v236
	v_fmamk_f32 v93, v93, 0x3dd53b94, v236
	v_fmamk_f32 v94, v94, 0x3dd53b94, v236
	v_fmamk_f32 v95, v95, 0x3dd53b94, v236
	v_mfma_f32_32x32x16_bf16 v[16:31], v[136:139], v[246:249], v[16:31]
	ds_read_b64_tr_b16 v[246:247], v174 offset:0x3600
	ds_read_b64_tr_b16 v[248:249], v174 offset:0x3e00
	v_exp_f32_e32 v222, v80
	v_exp_f32_e32 v224, v81
	v_exp_f32_e32 v220, v82
	v_mfma_f32_32x32x16_bf16 v[16:31], v[208:211], v[250:253], v[16:31]
	v_exp_f32_e32 v223, v83
	v_exp_f32_e32 v219, v84
	v_exp_f32_e32 v221, v85
	s_waitcnt lgkmcnt(0)
	v_mfma_f32_32x32x16_bf16 v[48:63], v[128:131], v[162:165], v[48:63]
	v_exp_f32_e32 v217, v86
	v_exp_f32_e32 v218, v87
	v_exp_f32_e32 v212, v88
	v_fmamk_f32 v130, v70, 0x3dd53b94, v236
	v_fmamk_f32 v131, v71, 0x3dd53b94, v236
	v_fmamk_f32 v128, v72, 0x3dd53b94, v236
	v_fmamk_f32 v129, v73, 0x3dd53b94, v236
	v_mfma_f32_32x32x16_bf16 v[48:63], v[132:135], v[238:241], v[48:63]
	v_exp_f32_e32 v214, v89
	v_exp_f32_e32 v213, v91
	v_exp_f32_e32 v207, v94
	v_fmamk_f32 v132, v68, 0x3dd53b94, v236
	v_fmamk_f32 v133, v69, 0x3dd53b94, v236
	v_fmamk_f32 v134, v78, 0x3dd53b94, v236
	v_fmamk_f32 v135, v79, 0x3dd53b94, v236
	v_mfma_f32_32x32x16_bf16 v[48:63], v[136:139], v[242:245], v[48:63]
	v_fmamk_f32 v138, v64, 0x3dd53b94, v236
	v_fmamk_f32 v139, v65, 0x3dd53b94, v236
	v_fmamk_f32 v136, v66, 0x3dd53b94, v236
	v_fmamk_f32 v137, v67, 0x3dd53b94, v236
	v_fmamk_f32 v162, v74, 0x3dd53b94, v236
	v_fmamk_f32 v163, v75, 0x3dd53b94, v236
	v_fmamk_f32 v160, v76, 0x3dd53b94, v236
	v_fmamk_f32 v161, v77, 0x3dd53b94, v236
	v_mfma_f32_32x32x16_bf16 v[48:63], v[208:211], v[246:249], v[48:63]
	v_exp_f32_e32 v211, v90
	v_exp_f32_e32 v208, v92
	v_exp_f32_e32 v210, v93
	v_exp_f32_e32 v209, v95
	v_add_f32_e32 v64, v203, v204
	v_fmac_f32_e32 v64, v197, v140
	v_add_f32_e32 v140, v215, v216
	s_addk_i32 s13, 0x80
	s_addk_i32 s14, 0x80
	v_fmac_f32_e32 v140, v64, v206
	s_cbranch_vccz .LBB0_2020
	s_and_saveexec_b64 s[10:11], s[4:5]
	ds_write_b32 v189, v205 offset:128
	s_or_b64 exec, exec, s[10:11]
	s_waitcnt lgkmcnt(0)
	v_add_u32_e32 v164, s12, v169
	ds_read_b128 v[238:241], v164 offset:224
	ds_read_b128 v[242:245], v164 offset:192
	ds_read_b128 v[246:249], v164 offset:160
	ds_read_b128 v[250:253], v164 offset:128
	s_waitcnt lgkmcnt(3)
	v_pk_mul_f32 v[12:13], v[12:13], v[238:239]
	s_waitcnt lgkmcnt(2)
	v_pk_mul_f32 v[8:9], v[8:9], v[242:243]
	s_waitcnt lgkmcnt(1)
	v_pk_mul_f32 v[4:5], v[4:5], v[246:247]
	v_pk_mul_f32 v[14:15], v[14:15], v[240:241]
	v_pk_mul_f32 v[10:11], v[10:11], v[244:245]
	v_pk_mul_f32 v[6:7], v[6:7], v[248:249]
	s_waitcnt lgkmcnt(0)
	v_pk_mul_f32 v[2:3], v[2:3], v[252:253]
	v_pk_mul_f32 v[0:1], v[0:1], v[250:251]
	v_pk_mul_f32 v[44:45], v[44:45], v[238:239]
	v_pk_mul_f32 v[40:41], v[40:41], v[242:243]
	v_pk_mul_f32 v[36:37], v[36:37], v[246:247]
	v_pk_mul_f32 v[46:47], v[46:47], v[240:241]
	v_pk_mul_f32 v[42:43], v[42:43], v[244:245]
	v_pk_mul_f32 v[38:39], v[38:39], v[248:249]
	v_pk_mul_f32 v[34:35], v[34:35], v[252:253]
	v_pk_mul_f32 v[32:33], v[32:33], v[250:251]
	v_pk_mul_f32 v[28:29], v[28:29], v[238:239]
	v_pk_mul_f32 v[24:25], v[24:25], v[242:243]
	v_pk_mul_f32 v[20:21], v[20:21], v[246:247]
	v_pk_mul_f32 v[30:31], v[30:31], v[240:241]
	v_pk_mul_f32 v[26:27], v[26:27], v[244:245]
	v_pk_mul_f32 v[22:23], v[22:23], v[248:249]
	v_pk_mul_f32 v[18:19], v[18:19], v[252:253]
	v_pk_mul_f32 v[16:17], v[16:17], v[250:251]
	v_pk_mul_f32 v[60:61], v[60:61], v[238:239]
	v_pk_mul_f32 v[56:57], v[56:57], v[242:243]
	v_pk_mul_f32 v[52:53], v[52:53], v[246:247]
	v_pk_mul_f32 v[62:63], v[62:63], v[240:241]
	v_pk_mul_f32 v[58:59], v[58:59], v[244:245]
	v_pk_mul_f32 v[54:55], v[54:55], v[248:249]
	v_pk_mul_f32 v[50:51], v[50:51], v[252:253]
	v_pk_mul_f32 v[48:49], v[48:49], v[250:251]
